# speedup vs baseline: 1.0926x; 1.0161x over previous
.LBB0_9:
	s_or_b64 exec, exec, s[8:9]
	v_add_u32_e32 v35, 0x5000, v27
	v_add_u32_e32 v34, 0x5000, v28
	v_add_u32_e32 v30, 0x5000, v30
	v_add_u32_e32 v28, 0x5000, v31
	v_add_u32_e32 v27, 0x5000, v32
	s_barrier
	s_and_saveexec_b64 s[4:5], vcc
	s_cbranch_execz .LBB0_12
	s_load_dwordx2 s[8:9], s[0:1], 0x10
	s_movk_i32 s3, 0x7d
	v_mov_b32_e32 v31, s2
	v_mad_u32_u24 v32, v0, s3, v31
	v_sub_u32_e32 v29, v33, v29
	v_ashrrev_i32_e32 v33, 31, v32
	s_waitcnt lgkmcnt(0)
	v_lshl_add_u64 v[32:33], v[32:33], 2, s[8:9]
	v_cmp_eq_u32_e32 vcc, 0, v0
	ds_write_b32 v1, v29 offset:20480
	global_store_dword v[32:33], v29, off sc1
	s_and_b64 exec, exec, vcc
	s_cbranch_execz .LBB0_12
	s_ashr_i32 s3, s2, 31
	s_lshl_b64 s[10:11], s[2:3], 2
	s_add_u32 s8, s8, s10
	s_addc_u32 s9, s9, s11
	v_mov_b32_e32 v29, 0x1f000
	v_mov_b32_e32 v31, 0x1400
	global_store_dword v29, v31, s[8:9] offset:1024 sc1

.LBB0_17:
	v_lshrrev_b32_e32 v3, 3, v7
	v_lshrrev_b32_e32 v20, 3, v6
	v_ashrrev_i32_e32 v21, 7, v7
	v_ashrrev_i32_e32 v22, 7, v6
	v_lshrrev_b32_e32 v23, 5, v7
	v_lshrrev_b32_e32 v24, 5, v6
	v_and_b32_e32 v21, 0xffffffe0, v21
	v_and_b32_e32 v22, 0xffffffe0, v22
	v_and_b32_e32 v3, 31, v3
	v_and_b32_e32 v20, 31, v20
	v_and_b32_e32 v25, 0x70, v23
	v_and_b32_e32 v26, 0x70, v24
	v_and_b32_e32 v23, 8, v23
	v_and_b32_e32 v24, 8, v24
	v_or_b32_e32 v3, v21, v3
	v_or_b32_e32 v20, v22, v20
	v_or_b32_e32 v21, v23, v1
	v_or_b32_e32 v22, v24, v4
	v_or_b32_e32 v21, v21, v25
	v_or_b32_e32 v22, v22, v26
	v_lshlrev_b32_e32 v23, 6, v3
	v_lshlrev_b32_e32 v24, 6, v20
	v_lshlrev_b32_e32 v27, 7, v20
	v_lshlrev_b32_e32 v3, 7, v3
	v_add3_u32 v28, v21, v23, s25
	v_or_b32_e32 v23, v23, v21
	v_cmp_gt_u32_e32 vcc, 64, v25
	v_add3_u32 v25, v22, v24, s25
	v_or_b32_e32 v24, v24, v22
	v_or_b32_e32 v22, v27, v22
	v_cmp_gt_u32_e64 s[2:3], 64, v26
	v_or_b32_e32 v20, v3, v21
	v_cndmask_b32_e32 v26, v28, v23, vcc
	v_cndmask_b32_e64 v24, v25, v24, s[2:3]
	v_ashrrev_i32_e32 v23, 31, v22
	v_cndmask_b32_e32 v29, v11, v12, vcc
	v_cndmask_b32_e32 v28, v13, v14, vcc
	v_cndmask_b32_e64 v31, v15, v16, s[2:3]
	v_cndmask_b32_e64 v30, v17, v18, s[2:3]
	v_ashrrev_i32_e32 v21, 31, v20
	v_ashrrev_i32_e32 v27, 31, v26
	v_ashrrev_i32_e32 v25, 31, v24
	v_lshl_add_u64 v[22:23], v[22:23], 2, s[16:17]
	v_lshl_add_u64 v[20:21], v[20:21], 2, s[16:17]
	v_lshl_add_u64 v[24:25], v[24:25], 2, v[30:31]
	v_lshl_add_u64 v[26:27], v[26:27], 2, v[28:29]
	global_load_dword v3, v[22:23], off
	global_load_dword v28, v[20:21], off
	global_load_dword v29, v[24:25], off
	global_load_dword v30, v[26:27], off
	v_ashrrev_i32_e32 v23, 31, v6
	v_mov_b32_e32 v22, v6
	v_add_u32_e32 v19, -2, v19
	v_ashrrev_i32_e32 v21, 31, v7
	v_mov_b32_e32 v20, v7
	v_lshlrev_b64 v[22:23], 1, v[22:23]
	v_cmp_eq_u32_e32 vcc, 0, v19
	v_add_u32_e32 v7, s24, v7
	v_add_u32_e32 v6, s13, v6
	v_lshlrev_b64 v[20:21], 1, v[20:21]
	v_lshl_add_u64 v[24:25], s[4:5], 0, v[22:23]
	v_lshl_add_u64 v[22:23], s[6:7], 0, v[22:23]
	s_or_b64 s[20:21], vcc, s[20:21]
	v_lshl_add_u64 v[26:27], s[4:5], 0, v[20:21]
	v_lshl_add_u64 v[20:21], s[6:7], 0, v[20:21]
	s_waitcnt vmcnt(2)
	v_cvt_pk_f16_f32 v3, v3, v28
	s_waitcnt vmcnt(0)
	v_cvt_pk_f16_f32 v28, v29, v30
	global_store_short v[22:23], v3, off sc1
	global_store_short_d16_hi v[20:21], v3, off sc1
	global_store_short v[24:25], v28, off sc1
	global_store_short_d16_hi v[26:27], v28, off sc1
	s_andn2_b64 exec, exec, s[20:21]
	s_cbranch_execnz .LBB0_17
	s_or_b64 exec, exec, s[20:21]
	v_mad_u64_u32 v[6:7], s[2:3], v9, s12, v[2:3]
	v_cmp_ne_u32_e32 vcc, v8, v9
	s_orn2_b64 s[2:3], vcc, exec

.LBB0_21:
	v_lshrrev_b32_e32 v12, 3, v6
	v_ashrrev_i32_e32 v13, 7, v6
	v_lshrrev_b32_e32 v14, 5, v6
	v_bfi_b32 v12, s13, v13, v12
	v_and_b32_e32 v13, 0x70, v14
	v_and_b32_e32 v14, 8, v14
	v_or3_b32 v14, v14, v4, v13
	v_lshlrev_b32_e32 v15, 6, v12
	v_add3_u32 v16, v14, v15, s20
	v_or_b32_e32 v15, v15, v14
	v_lshl_or_b32 v12, v12, 7, v14
	v_cmp_gt_u32_e32 vcc, 64, v13
	v_ashrrev_i32_e32 v13, 31, v12
	v_lshl_add_u64 v[12:13], v[12:13], 2, s[16:17]
	v_cndmask_b32_e32 v14, v16, v15, vcc
	v_cndmask_b32_e32 v17, v1, v3, vcc
	v_cndmask_b32_e32 v16, v7, v11, vcc
	v_ashrrev_i32_e32 v15, 31, v14
	v_lshl_add_u64 v[14:15], v[14:15], 2, v[16:17]
	global_load_dword v16, v[12:13], off
	global_load_dword v17, v[14:15], off
	v_add_u32_e32 v6, s12, v6
	v_cmp_lt_i32_e32 vcc, s8, v6
	v_lshl_add_u64 v[12:13], s[4:5], 0, v[8:9]
	v_lshl_add_u64 v[14:15], s[6:7], 0, v[8:9]
	v_lshl_add_u64 v[8:9], v[8:9], 0, s[2:3]
	s_or_b64 s[18:19], vcc, s[18:19]
	s_waitcnt vmcnt(1)
	v_cvt_f16_f32_e32 v16, v16
	s_waitcnt vmcnt(0)
	v_cvt_f16_f32_e32 v17, v17
	global_store_short v[14:15], v16, off sc1
	global_store_short v[12:13], v17, off sc1
	s_andn2_b64 exec, exec, s[18:19]
	s_cbranch_execnz .LBB0_21
.LBB0_22:
	s_or_b64 exec, exec, s[14:15]
	s_movk_i32 s2, 0x80
	v_cmp_gt_i32_e32 vcc, s2, v2
	s_and_saveexec_b64 s[2:3], vcc
	s_cbranch_execz .LBB0_24
	s_waitcnt lgkmcnt(0)
	s_load_dwordx4 s[4:7], s[0:1], 0x38
	v_mov_b32_e32 v3, 0
	v_lshlrev_b64 v[6:7], 2, v[2:3]
	s_waitcnt lgkmcnt(0)
	v_lshl_add_u64 v[12:13], s[4:5], 0, v[6:7]
	v_lshl_add_u64 v[8:9], s[6:7], 0, v[6:7]
	global_load_dword v1, v[12:13], off
	global_load_dword v3, v[8:9], off
	s_load_dwordx2 s[4:5], s[0:1], 0x58
	s_waitcnt lgkmcnt(0)
	v_lshl_add_u64 v[6:7], s[4:5], 0, v[6:7]
	s_waitcnt vmcnt(0)
	v_add_f32_e32 v1, v1, v3
	global_store_dword v[6:7], v1, off sc1

.LBB0_27:
	v_add_u32_e32 v7, -2, v7
	v_ashrrev_i32_e32 v9, 31, v1
	v_mov_b32_e32 v8, v1
	v_ashrrev_i32_e32 v11, 31, v0
	v_mov_b32_e32 v10, v0
	v_cmp_eq_u32_e32 vcc, 0, v7
	v_add_u32_e32 v1, s11, v1
	v_add_u32_e32 v0, s10, v0
	s_waitcnt lgkmcnt(0)
	v_lshl_add_u64 v[10:11], v[10:11], 2, s[6:7]
	v_lshl_add_u64 v[8:9], v[8:9], 2, s[6:7]
	s_or_b64 s[8:9], vcc, s[8:9]
	global_store_dword v[10:11], v6, off sc1
	global_store_dword v[8:9], v6, off sc1
	s_andn2_b64 exec, exec, s[8:9]
	s_cbranch_execnz .LBB0_27
	s_or_b64 exec, exec, s[8:9]
	v_mad_u64_u32 v[0:1], s[8:9], v5, s12, v[2:3]
	v_cmp_ne_u32_e32 vcc, v4, v5
	s_orn2_b64 s[8:9], vcc, exec

.LBB0_31:
	v_add_u32_e32 v0, s12, v0
	v_cmp_lt_i32_e32 vcc, s8, v0
	global_store_dword v[4:5], v1, off sc1
	s_or_b64 s[6:7], vcc, s[6:7]
	v_lshl_add_u64 v[4:5], v[4:5], 0, s[2:3]
	s_andn2_b64 exec, exec, s[6:7]
	s_cbranch_execnz .LBB0_31
.LBB0_32:
	s_or_b64 exec, exec, s[4:5]
	v_cmp_gt_i32_e32 vcc, 64, v2
	s_and_saveexec_b64 s[2:3], vcc
	s_cbranch_execz .LBB0_34
	s_load_dwordx2 s[4:5], s[0:1], 0x68
	v_mov_b32_e32 v3, 0
	s_waitcnt lgkmcnt(0)
	v_lshl_add_u64 v[0:1], v[2:3], 1, s[4:5]
	v_add_co_u32_e32 v0, vcc, 0x61a000, v0
	s_nop 1
	v_addc_co_u32_e32 v1, vcc, 0, v1, vcc
	global_store_short v[0:1], v3, off offset:2048 sc1
.LBB0_34:
	s_or_b64 exec, exec, s[2:3]
	v_cmp_gt_i32_e32 vcc, 32, v2
	s_and_saveexec_b64 s[2:3], vcc
	s_cbranch_execz .LBB0_36
	s_load_dwordx2 s[0:1], s[0:1], 0x70
	v_mov_b32_e32 v3, 0
	s_waitcnt lgkmcnt(0)
	v_lshl_add_u64 v[0:1], v[2:3], 2, s[0:1]
	v_add_co_u32_e32 v0, vcc, 0x61a000, v0
	s_nop 1
	v_addc_co_u32_e32 v1, vcc, 0, v1, vcc
	global_store_dword v[0:1], v3, off offset:2048 sc1

.LBB1_24:
	s_or_b64 exec, exec, s[12:13]
	v_mov_b32_e32 v18, 0
	s_waitcnt lgkmcnt(0)
	s_barrier
	ds_read_b64 v[30:31], v18 offset:22528
	s_and_saveexec_b64 s[10:11], s[8:9]
	v_lshlrev_b32_e32 v18, 2, v0
	ds_read_b32 v18, v18 offset:16384
	s_or_b64 exec, exec, s[10:11]
	v_mbcnt_lo_u32_b32 v19, -1, 0
	v_mbcnt_hi_u32_b32 v21, -1, v19
	v_and_b32_e32 v20, 64, v21
	v_add_u32_e32 v19, -1, v21
	v_cmp_lt_i32_e64 s[10:11], v19, v20
	v_and_b32_e32 v38, 63, v0
	v_add_u32_e32 v39, -2, v21
	v_cndmask_b32_e64 v19, v19, v21, s[10:11]
	v_lshlrev_b32_e32 v19, 2, v19
	s_waitcnt lgkmcnt(0)
	ds_bpermute_b32 v19, v19, v18
	v_cmp_ne_u32_e64 s[10:11], 0, v38
	s_waitcnt lgkmcnt(0)
	s_nop 0
	v_cndmask_b32_e64 v19, 0, v19, s[10:11]
	v_cmp_lt_i32_e64 s[10:11], v39, v20
	v_add_u32_e32 v19, v19, v18
	s_nop 0
	v_cndmask_b32_e64 v39, v39, v21, s[10:11]
	v_lshlrev_b32_e32 v39, 2, v39
	ds_bpermute_b32 v39, v39, v19
	v_cmp_lt_u32_e64 s[10:11], 1, v38
	s_waitcnt lgkmcnt(0)
	s_nop 0
	v_cndmask_b32_e64 v39, 0, v39, s[10:11]
	v_add_u32_e32 v19, v39, v19
	v_add_u32_e32 v39, -4, v21
	v_cmp_lt_i32_e64 s[10:11], v39, v20
	s_nop 1
	v_cndmask_b32_e64 v39, v39, v21, s[10:11]
	v_lshlrev_b32_e32 v39, 2, v39
	ds_bpermute_b32 v39, v39, v19
	v_cmp_lt_u32_e64 s[10:11], 3, v38
	s_waitcnt lgkmcnt(0)
	s_nop 0
	v_cndmask_b32_e64 v39, 0, v39, s[10:11]
	v_add_u32_e32 v19, v39, v19
	v_add_u32_e32 v39, -8, v21
	v_cmp_lt_i32_e64 s[10:11], v39, v20
	s_nop 1
	v_cndmask_b32_e64 v39, v39, v21, s[10:11]
	v_lshlrev_b32_e32 v39, 2, v39
	ds_bpermute_b32 v39, v39, v19
	v_cmp_lt_u32_e64 s[10:11], 7, v38
	s_waitcnt lgkmcnt(0)
	s_nop 0
	v_cndmask_b32_e64 v39, 0, v39, s[10:11]
	v_add_u32_e32 v19, v39, v19
	v_add_u32_e32 v39, -16, v21
	v_cmp_lt_i32_e64 s[10:11], v39, v20
	s_nop 1
	v_cndmask_b32_e64 v39, v39, v21, s[10:11]
	v_lshlrev_b32_e32 v39, 2, v39
	ds_bpermute_b32 v39, v39, v19
	v_cmp_lt_u32_e64 s[10:11], 15, v38
	s_waitcnt lgkmcnt(0)
	s_nop 0
	v_cndmask_b32_e64 v39, 0, v39, s[10:11]
	v_add_u32_e32 v19, v39, v19
	v_subrev_u32_e32 v39, 32, v21
	v_cmp_lt_i32_e64 s[10:11], v39, v20
	s_nop 1
	v_cndmask_b32_e64 v39, v39, v21, s[10:11]
	v_lshlrev_b32_e32 v39, 2, v39
	ds_bpermute_b32 v39, v39, v19
	v_cmp_gt_u32_e64 s[10:11], 32, v38
	s_waitcnt lgkmcnt(0)
	s_nop 0
	v_cndmask_b32_e64 v39, v39, 0, s[10:11]
	v_add_u32_e32 v19, v39, v19
	v_and_b32_e32 v39, 0x33f, v0
	v_cmp_eq_u32_e64 s[12:13], 63, v39
	s_and_saveexec_b64 s[14:15], s[12:13]
	v_and_b32_e32 v39, 60, v25
	ds_write_b32 v39, v19 offset:20480
	s_or_b64 exec, exec, s[14:15]
	s_waitcnt lgkmcnt(0)
	s_barrier
	s_and_saveexec_b64 s[18:19], s[8:9]
	s_cbranch_execz .LBB1_31
	v_mov_b32_e32 v39, 0
	ds_read_b96 v[40:42], v39 offset:20480
	s_movk_i32 s14, 0x7f
	v_cmp_lt_u32_e64 s[12:13], 63, v0
	v_sub_u32_e32 v19, v19, v18
	s_waitcnt lgkmcnt(0)
	v_cndmask_b32_e64 v39, 0, v40, s[12:13]
	v_cmp_lt_u32_e64 s[12:13], s14, v0
	v_add_u32_e32 v19, v19, v39
	s_nop 0
	v_cndmask_b32_e64 v40, 0, v41, s[12:13]
	s_movk_i32 s12, 0xbf
	v_cmp_lt_u32_e64 s[12:13], s12, v0
	s_nop 1
	v_cndmask_b32_e64 v41, 0, v42, s[12:13]
	v_add_co_u32_e64 v18, s[12:13], 1, v18
	v_cvt_f32_u32_e32 v18, v18
	v_add3_u32 v19, v19, v40, v41
	v_lshlrev_b32_e32 v40, 2, v0
	v_rsq_f32_e32 v39, v18
	v_add_u32_e32 v18, v19, v30
	ds_write_b32 v40, v18 offset:21504
	v_add_u32_e32 v18, s3, v0
	v_mul_f32_e32 v41, 0x45800000, v39
	s_movk_i32 s3, 0xc4
	v_cndmask_b32_e64 v39, v39, v41, s[12:13]
	v_cmp_gt_u32_e64 s[12:13], s3, v0
	s_mov_b32 s3, 0xc350
	v_cmp_gt_i32_e64 s[14:15], s3, v18
	s_and_b64 s[12:13], s[12:13], s[14:15]
	ds_write2st64_b32 v40, v19, v39 offset0:68 offset1:76
	s_and_b64 exec, exec, s[12:13]
	s_cbranch_execz .LBB1_31
	v_ashrrev_i32_e32 v19, 31, v18
	v_lshl_add_u64 v[18:19], v[18:19], 2, s[30:31]
	global_store_dword v[18:19], v39, off sc1

.LBB1_37:
	s_or_b64 exec, exec, s[8:9]
	v_lshl_or_b32 v38, v39, 5, v38
	v_ashrrev_i32_e32 v39, 31, v38
	v_lshl_add_u64 v[38:39], v[38:39], 4, s[36:37]
	s_waitcnt lgkmcnt(0)
	global_store_dwordx4 v[38:39], v[18:21], off sc1
.LBB1_38:
	s_or_b64 exec, exec, s[30:31]
	s_and_saveexec_b64 s[8:9], s[6:7]
	s_cbranch_execz .LBB1_43
	v_mov_b32_e32 v18, 2
	v_lshlrev_b32_sdwa v19, v18, v37 dst_sel:DWORD dst_unused:UNUSED_PAD src0_sel:DWORD src1_sel:WORD_1
	v_mov_b32_e32 v18, 1
	ds_add_rtn_u32 v18, v19, v18 offset:17408
	ds_read_b32 v19, v19 offset:18432
	v_and_b32_e32 v20, 0xffff, v37
	s_movk_i32 s2, 0xfff
	s_waitcnt lgkmcnt(1)
	v_cmp_lt_u32_e64 s[2:3], s2, v18
	s_waitcnt lgkmcnt(0)
	v_lshl_or_b32 v19, v19, 16, v20
	s_and_saveexec_b64 s[6:7], s[2:3]
	s_xor_b64 s[2:3], exec, s[6:7]
	s_cbranch_execz .LBB1_41
	v_add_u32_e32 v20, v18, v30
	v_mov_b32_e32 v21, 0
	v_lshl_add_u64 v[20:21], v[20:21], 2, s[28:29]
	global_store_dword v[20:21], v19, off sc1

.LBB1_43:
	s_or_b64 exec, exec, s[8:9]
	s_and_saveexec_b64 s[6:7], s[4:5]
	s_cbranch_execz .LBB1_48
	v_mov_b32_e32 v18, 2
	v_lshlrev_b32_sdwa v19, v18, v36 dst_sel:DWORD dst_unused:UNUSED_PAD src0_sel:DWORD src1_sel:WORD_1
	v_mov_b32_e32 v18, 1
	ds_add_rtn_u32 v18, v19, v18 offset:17408
	ds_read_b32 v19, v19 offset:18432
	v_and_b32_e32 v20, 0xffff, v36
	s_movk_i32 s2, 0xfff
	s_waitcnt lgkmcnt(1)
	v_cmp_lt_u32_e64 s[2:3], s2, v18
	s_waitcnt lgkmcnt(0)
	v_lshl_or_b32 v19, v19, 16, v20
	s_and_saveexec_b64 s[4:5], s[2:3]
	s_xor_b64 s[2:3], exec, s[4:5]
	s_cbranch_execz .LBB1_46
	v_add_u32_e32 v20, v18, v30
	v_mov_b32_e32 v21, 0
	v_lshl_add_u64 v[20:21], v[20:21], 2, s[28:29]
	global_store_dword v[20:21], v19, off sc1

.LBB1_48:
	s_or_b64 exec, exec, s[6:7]
	s_and_saveexec_b64 s[4:5], s[16:17]
	s_cbranch_execz .LBB1_53
	v_mov_b32_e32 v18, 2
	v_lshlrev_b32_sdwa v19, v18, v35 dst_sel:DWORD dst_unused:UNUSED_PAD src0_sel:DWORD src1_sel:WORD_1
	v_mov_b32_e32 v18, 1
	ds_add_rtn_u32 v18, v19, v18 offset:17408
	ds_read_b32 v19, v19 offset:18432
	v_and_b32_e32 v20, 0xffff, v35
	s_movk_i32 s2, 0xfff
	s_waitcnt lgkmcnt(1)
	v_cmp_lt_u32_e64 s[2:3], s2, v18
	s_waitcnt lgkmcnt(0)
	v_lshl_or_b32 v19, v19, 16, v20
	s_and_saveexec_b64 s[6:7], s[2:3]
	s_xor_b64 s[2:3], exec, s[6:7]
	s_cbranch_execz .LBB1_51
	v_add_u32_e32 v20, v18, v30
	v_mov_b32_e32 v21, 0
	v_lshl_add_u64 v[20:21], v[20:21], 2, s[28:29]
	global_store_dword v[20:21], v19, off sc1

.LBB1_53:
	s_or_b64 exec, exec, s[4:5]
	s_and_saveexec_b64 s[2:3], s[0:1]
	s_cbranch_execz .LBB1_58
	v_mov_b32_e32 v18, 2
	v_lshlrev_b32_sdwa v19, v18, v34 dst_sel:DWORD dst_unused:UNUSED_PAD src0_sel:DWORD src1_sel:WORD_1
	v_mov_b32_e32 v18, 1
	ds_add_rtn_u32 v18, v19, v18 offset:17408
	ds_read_b32 v19, v19 offset:18432
	v_and_b32_e32 v20, 0xffff, v34
	s_movk_i32 s0, 0xfff
	s_waitcnt lgkmcnt(1)
	v_cmp_lt_u32_e64 s[0:1], s0, v18
	s_waitcnt lgkmcnt(0)
	v_lshl_or_b32 v19, v19, 16, v20
	s_and_saveexec_b64 s[4:5], s[0:1]
	s_xor_b64 s[0:1], exec, s[4:5]
	s_cbranch_execz .LBB1_56
	v_add_u32_e32 v20, v18, v30
	v_mov_b32_e32 v21, 0
	v_lshl_add_u64 v[20:21], v[20:21], 2, s[28:29]
	global_store_dword v[20:21], v19, off sc1

.LBB1_61:
	v_add_u32_e32 v18, v27, v33
	v_lshl_add_u64 v[34:35], v[18:19], 2, s[26:27]
	global_load_dword v34, v[34:35], off
	s_waitcnt vmcnt(0)
	v_lshlrev_b32_sdwa v35, v21, v34 dst_sel:DWORD dst_unused:UNUSED_PAD src0_sel:DWORD src1_sel:WORD_1
	ds_add_rtn_u32 v18, v35, v20 offset:17408
	ds_read_b32 v35, v35 offset:18432
	v_and_b32_e32 v34, 0xffff, v34
	s_waitcnt lgkmcnt(1)
	v_cmp_lt_u32_e32 vcc, s6, v18
	s_waitcnt lgkmcnt(0)
	v_lshl_or_b32 v34, v35, 16, v34
	s_and_saveexec_b64 s[4:5], vcc
	s_xor_b64 s[4:5], exec, s[4:5]
	s_cbranch_execz .LBB1_63
	v_add_u32_e32 v18, v18, v30
	v_lshl_add_u64 v[36:37], v[18:19], 2, s[28:29]
	global_store_dword v[36:37], v34, off sc1

.LBB2_28:
	s_or_b64 exec, exec, s[0:1]
	s_waitcnt lgkmcnt(0)
	v_mov_b32_e32 v28, 0
	s_barrier
	ds_read_b128 v[30:33], v28 offset:36096
	v_cmp_eq_u32_e32 vcc, 0, v0
	s_waitcnt lgkmcnt(0)
	v_max_f32_e32 v27, v33, v33
	v_max_f32_e32 v29, v32, v32
	v_max_f32_e32 v27, v29, v27
	v_max3_f32 v27, v30, v31, v27
	s_and_saveexec_b64 s[0:1], vcc
	s_cbranch_execz .LBB2_30
	s_ashr_i32 s21, s20, 31
	s_lshl_b64 s[6:7], s[20:21], 2
	s_add_u32 s6, s22, s6
	s_addc_u32 s7, s23, s7
	v_mul_f32_e32 v29, 0x3b808081, v27
	global_store_dword v28, v29, s[6:7] sc1
